# C1 combine: gate vectors of both halves issued before the next-row prefetch and waited by count (vmcnt 14/15) instead of vmcnt(0), so the prefetch is not drained at the first multiply
# speedup vs baseline: 1.0030x; 1.0030x over previous
.LBB0_3036:
	s_add_i32 s10, s6, 0x800
	s_cmp_lt_i32 s10, s36
	s_cselect_b64 s[12:13], -1, 0
	s_and_b64 s[14:15], s[12:13], exec
	s_cselect_b32 s14, s10, s6
	s_ashr_i32 s15, s14, 31
	s_lshl_b64 s[16:17], s[14:15], 13
	v_lshl_add_u64 v[50:51], v[118:119], 0, s[16:17]
	s_movk_i32 s4, 0x1000
	v_add_co_u32_e32 v52, vcc, s4, v50
	s_min_i32 s4, s6, 0x4000
	s_lshl_b64 s[14:15], s[14:15], 12
	s_ashr_i32 s4, s4, 12
	s_waitcnt vmcnt(9)
	v_lshlrev_b32_e32 v100, 16, v2
	v_and_b32_e32 v101, 0xffff0000, v2
	v_lshlrev_b32_e32 v102, 16, v3
	v_and_b32_e32 v103, 0xffff0000, v3
	v_lshl_add_u64 v[54:55], v[120:121], 0, s[14:15]
	s_mul_hi_i32 s15, s4, 0x1800
	s_mul_i32 s14, s4, 0x1800
	v_pk_add_f32 v[102:103], v[102:103], 0 op_sel_hi:[1,0]
	v_pk_add_f32 v[100:101], v[100:101], 0 op_sel_hi:[1,0]
	v_lshlrev_b32_e32 v104, 16, v4
	v_and_b32_e32 v105, 0xffff0000, v4
	v_lshlrev_b32_e32 v106, 16, v5
	v_and_b32_e32 v107, 0xffff0000, v5
	s_waitcnt vmcnt(7)
	v_lshlrev_b32_e32 v108, 16, v14
	v_and_b32_e32 v109, 0xffff0000, v14
	v_lshlrev_b32_e32 v110, 16, v15
	v_and_b32_e32 v111, 0xffff0000, v15
	s_lshl_b64 s[14:15], s[14:15], 2
	v_pk_add_f32 v[106:107], v[106:107], 0 op_sel_hi:[1,0]
	v_pk_add_f32 v[104:105], v[104:105], 0 op_sel_hi:[1,0]
	v_pk_add_f32 v[100:101], v[100:101], v[108:109]
	v_pk_add_f32 v[102:103], v[102:103], v[110:111]
	v_lshlrev_b32_e32 v108, 16, v16
	v_and_b32_e32 v109, 0xffff0000, v16
	v_lshlrev_b32_e32 v110, 16, v17
	v_and_b32_e32 v111, 0xffff0000, v17
	s_add_u32 s4, s37, s14
	v_pk_add_f32 v[104:105], v[104:105], v[108:109]
	v_pk_add_f32 v[106:107], v[106:107], v[110:111]
	s_waitcnt vmcnt(5)
	v_lshlrev_b32_e32 v108, 16, v18
	v_and_b32_e32 v109, 0xffff0000, v18
	v_lshlrev_b32_e32 v110, 16, v19
	v_and_b32_e32 v111, 0xffff0000, v19
	s_addc_u32 s7, s38, s15
	v_pk_add_f32 v[102:103], v[102:103], v[110:111]
	v_pk_add_f32 v[100:101], v[100:101], v[108:109]
	v_lshlrev_b32_e32 v108, 16, v20
	v_and_b32_e32 v109, 0xffff0000, v20
	v_lshlrev_b32_e32 v110, 16, v21
	v_and_b32_e32 v111, 0xffff0000, v21
	s_add_u32 s16, s4, 0x5000
	v_pk_add_f32 v[106:107], v[106:107], v[110:111]
	v_pk_add_f32 v[104:105], v[104:105], v[108:109]
	s_waitcnt vmcnt(3)
	v_lshlrev_b32_e32 v108, 16, v26
	v_and_b32_e32 v109, 0xffff0000, v26
	v_lshlrev_b32_e32 v110, 16, v27
	v_and_b32_e32 v111, 0xffff0000, v27
	v_addc_co_u32_e32 v53, vcc, 0, v51, vcc
	s_addc_u32 s17, s7, 0
	v_pk_add_f32 v[100:101], v[100:101], v[108:109]
	v_pk_add_f32 v[112:113], v[102:103], v[110:111]
	v_lshlrev_b32_e32 v102, 16, v28
	v_and_b32_e32 v103, 0xffff0000, v28
	v_lshlrev_b32_e32 v108, 16, v29
	v_and_b32_e32 v109, 0xffff0000, v29
	v_lshlrev_b32_e32 v117, 2, v116
	v_lshlrev_b32_e32 v123, 2, v122
	v_pk_add_f32 v[114:115], v[104:105], v[102:103]
	v_pk_add_f32 v[130:131], v[106:107], v[108:109]
	global_load_dwordx4 v[108:111], v117, s[16:17] offset:16
	global_load_dwordx4 v[102:105], v117, s[16:17]
	global_load_dwordx4 v[154:157], v123, s[16:17] offset:16
	global_load_dwordx4 v[158:161], v123, s[16:17]
	global_load_dwordx4 v[94:97], v[50:51], off nt
	global_load_dwordx4 v[90:93], v[50:51], off offset:2048 nt
	global_load_dwordx4 v[86:89], v[52:53], off nt
	global_load_dwordx4 v[82:85], v[52:53], off offset:2048 nt
	global_load_dwordx4 v[74:77], v[54:55], off offset:16
	global_load_dwordx4 v[78:81], v[54:55], off
	global_load_dwordx4 v[70:73], v[50:51], off offset:1024 nt
	global_load_dwordx4 v[66:69], v[50:51], off offset:3072 nt
	global_load_dwordx4 v[62:65], v[52:53], off offset:1024 nt
	global_load_dwordx4 v[58:61], v[52:53], off offset:3072 nt
	s_nop 0
	global_load_dwordx4 v[50:53], v[54:55], off offset:2064
	s_nop 0
	global_load_dwordx4 v[54:57], v[54:55], off offset:2048
	v_lshlrev_b32_e32 v132, 16, v30
	v_and_b32_e32 v133, 0xffff0000, v30
	v_lshlrev_b32_e32 v134, 16, v31
	v_and_b32_e32 v135, 0xffff0000, v31
	s_ashr_i32 s7, s6, 31
	s_lshl_b64 s[18:19], s[6:7], 12
	v_cndmask_b32_e64 v98, 0, 1, s[8:9]
	v_cmp_ne_u32_e64 s[34:35], 1, v98
	s_andn2_b64 vcc, exec, s[8:9]
	s_waitcnt vmcnt(14)
	v_pk_fma_f32 v[106:107], v[112:113], v[104:105], v[12:13]
	v_pk_fma_f32 v[104:105], v[100:101], v[102:103], v[10:11]
	v_pk_fma_f32 v[102:103], v[130:131], v[110:111], v[8:9]
	v_pk_fma_f32 v[100:101], v[114:115], v[108:109], v[6:7]
	v_lshlrev_b32_e32 v108, 16, v22
	v_and_b32_e32 v109, 0xffff0000, v22
	v_lshlrev_b32_e32 v110, 16, v23
	v_and_b32_e32 v111, 0xffff0000, v23
	v_pk_add_f32 v[110:111], v[110:111], 0 op_sel_hi:[1,0]
	v_pk_add_f32 v[108:109], v[108:109], 0 op_sel_hi:[1,0]
	v_lshlrev_b32_e32 v112, 16, v24
	v_and_b32_e32 v113, 0xffff0000, v24
	v_lshlrev_b32_e32 v114, 16, v25
	v_and_b32_e32 v115, 0xffff0000, v25
	v_pk_add_f32 v[114:115], v[114:115], 0 op_sel_hi:[1,0]
	v_pk_add_f32 v[112:113], v[112:113], 0 op_sel_hi:[1,0]
	v_pk_add_f32 v[108:109], v[108:109], v[132:133]
	v_pk_add_f32 v[110:111], v[110:111], v[134:135]
	v_lshlrev_b32_e32 v132, 16, v32
	v_and_b32_e32 v133, 0xffff0000, v32
	v_lshlrev_b32_e32 v134, 16, v33
	v_and_b32_e32 v135, 0xffff0000, v33
	v_pk_add_f32 v[112:113], v[112:113], v[132:133]
	v_pk_add_f32 v[114:115], v[114:115], v[134:135]
	v_lshlrev_b32_e32 v132, 16, v34
	v_and_b32_e32 v133, 0xffff0000, v34
	v_lshlrev_b32_e32 v134, 16, v35
	v_and_b32_e32 v135, 0xffff0000, v35
	v_pk_add_f32 v[110:111], v[110:111], v[134:135]
	v_pk_add_f32 v[108:109], v[108:109], v[132:133]
	v_lshlrev_b32_e32 v132, 16, v36
	v_and_b32_e32 v133, 0xffff0000, v36
	v_lshlrev_b32_e32 v134, 16, v37
	v_and_b32_e32 v135, 0xffff0000, v37
	v_lshl_add_u64 v[130:131], v[126:127], 0, s[18:19]
	v_pk_add_f32 v[114:115], v[114:115], v[134:135]
	v_pk_add_f32 v[112:113], v[112:113], v[132:133]
	v_lshlrev_b32_e32 v132, 16, v38
	v_and_b32_e32 v133, 0xffff0000, v38
	v_lshlrev_b32_e32 v134, 16, v39
	v_and_b32_e32 v135, 0xffff0000, v39
	global_store_dwordx4 v[130:131], v[104:107], off
	global_store_dwordx4 v[130:131], v[100:103], off offset:16
	v_pk_add_f32 v[132:133], v[108:109], v[132:133]
	v_pk_add_f32 v[134:135], v[110:111], v[134:135]
	v_lshlrev_b32_e32 v108, 16, v40
	v_and_b32_e32 v109, 0xffff0000, v40
	v_lshlrev_b32_e32 v110, 16, v41
	v_and_b32_e32 v111, 0xffff0000, v41
	v_pk_add_f32 v[136:137], v[112:113], v[108:109]
	v_pk_add_f32 v[138:139], v[114:115], v[110:111]
	s_waitcnt vmcnt(14)
	v_pk_fma_f32 v[110:111], v[138:139], v[156:157], v[44:45]
	v_pk_fma_f32 v[114:115], v[134:135], v[160:161], v[48:49]
	v_pk_fma_f32 v[112:113], v[132:133], v[158:159], v[46:47]
	v_pk_fma_f32 v[108:109], v[136:137], v[154:155], v[42:43]
	global_store_dwordx4 v[130:131], v[112:115], off offset:2048
	global_store_dwordx4 v[130:131], v[108:111], off offset:2064
	s_cbranch_vccnz .LBB0_3038
	v_pk_mul_f32 v[130:131], v[106:107], v[106:107]
	v_pk_mul_f32 v[132:133], v[104:105], v[104:105]
	v_mul_f32_e32 v98, v108, v108
	v_pk_mov_b32 v[134:135], v[132:133], v[130:131] op_sel:[1,0]
	v_mov_b32_e32 v133, v131
	v_pk_add_f32 v[130:131], v[134:135], v[132:133]
	v_pk_mul_f32 v[132:133], v[102:103], v[102:103]
	v_pk_mul_f32 v[134:135], v[100:101], v[100:101]
	v_pk_add_f32 v[130:131], v[130:131], v[130:131] op_sel:[0,1] op_sel_hi:[1,0]
	v_pk_mov_b32 v[136:137], v[134:135], v[132:133] op_sel:[1,0]
	v_mov_b32_e32 v135, v133
	v_pk_add_f32 v[132:133], v[136:137], v[134:135]
	v_mul_f32_e32 v134, v109, v109
	v_pk_add_f32 v[132:133], v[132:133], v[132:133] op_sel:[0,1] op_sel_hi:[1,0]
	v_mov_b32_e32 v131, v98
	v_mov_b32_e32 v133, v134
	v_mul_f32_e32 v98, v113, v113
	v_mul_f32_e32 v135, v110, v110
	v_pk_add_f32 v[130:131], v[130:131], v[132:133]
	v_pk_fma_f32 v[132:133], v[112:113], v[112:113], v[98:99] op_sel_hi:[1,1,0]
	v_mul_f32_e32 v98, v115, v115
	v_mul_f32_e32 v136, v111, v111
	v_mov_b32_e32 v133, v135
	v_pk_fma_f32 v[134:135], v[114:115], v[114:115], v[98:99] op_sel_hi:[1,1,0]
	s_add_u32 s14, s39, s14
	v_mov_b32_e32 v135, v136
	v_pk_add_f32 v[132:133], v[132:133], v[134:135]
	s_addc_u32 s15, s40, s15
	v_pk_add_f32 v[130:131], v[130:131], v[132:133]
	s_add_u32 s16, s14, 0x1000
	v_add_f32_e32 v98, v130, v131
	v_and_b32_e32 v131, 64, v214
	v_xor_b32_e32 v130, 16, v214
	v_add_f32_dpp v98, v98, v98 quad_perm:[1,0,3,2] row_mask:0xf bank_mask:0xf bound_ctrl:1
	v_add_u32_e32 v131, 64, v131
	v_cmp_lt_i32_e32 vcc, v130, v131
	v_add_f32_dpp v98, v98, v98 quad_perm:[2,3,0,1] row_mask:0xf bank_mask:0xf bound_ctrl:1
	s_addc_u32 s17, s15, 0
	v_cndmask_b32_e32 v130, v214, v130, vcc
	v_add_f32_dpp v98, v98, v98 row_half_mirror row_mask:0xf bank_mask:0xf bound_ctrl:1
	v_lshlrev_b32_e32 v130, 2, v130
	s_lshl_b64 s[18:19], s[6:7], 11
	v_add_f32_dpp v98, v98, v98 row_mirror row_mask:0xf bank_mask:0xf bound_ctrl:1
	ds_bpermute_b32 v130, v130, v98
	s_waitcnt lgkmcnt(0)
	v_add_f32_e32 v98, v98, v130
	v_xor_b32_e32 v130, 32, v214
	v_cmp_lt_i32_e32 vcc, v130, v131
	s_nop 1
	v_cndmask_b32_e32 v130, v214, v130, vcc
	v_lshlrev_b32_e32 v130, 2, v130
	ds_bpermute_b32 v130, v130, v98
	s_waitcnt lgkmcnt(0)
	v_add_f32_e32 v98, v98, v130
	v_fmamk_f32 v98, v98, 0x3a800000, v1
	v_cmp_gt_f32_e32 vcc, s77, v98
	v_mul_f32_e32 v130, 0x4b800000, v98
	s_nop 0
	v_cndmask_b32_e32 v98, v98, v130, vcc
	v_rsq_f32_e32 v98, v98
	s_nop 0
	v_mul_f32_e32 v130, 0x45800000, v98
	v_cndmask_b32_e32 v98, v98, v130, vcc
	global_load_dwordx4 v[130:133], v[124:125], off offset:16
	global_load_dwordx4 v[134:137], v[124:125], off
	global_load_dwordx4 v[138:141], v117, s[16:17] offset:16
	global_load_dwordx4 v[142:145], v117, s[16:17]
	global_load_dwordx4 v[146:149], v117, s[14:15] offset:16
	global_load_dwordx4 v[150:153], v117, s[14:15]
	v_pk_mul_f32 v[106:107], v[106:107], v[98:99] op_sel_hi:[1,0]
	v_pk_mul_f32 v[104:105], v[104:105], v[98:99] op_sel_hi:[1,0]
	v_pk_mul_f32 v[102:103], v[102:103], v[98:99] op_sel_hi:[1,0]
	v_pk_mul_f32 v[100:101], v[100:101], v[98:99] op_sel_hi:[1,0]
	v_pk_mul_f32 v[114:115], v[114:115], v[98:99] op_sel_hi:[1,0]
	v_pk_mul_f32 v[112:113], v[112:113], v[98:99] op_sel_hi:[1,0]
	v_pk_mul_f32 v[110:111], v[110:111], v[98:99] op_sel_hi:[1,0]
	v_pk_mul_f32 v[108:109], v[108:109], v[98:99] op_sel_hi:[1,0]
	s_waitcnt vmcnt(5)
	v_pk_mul_f32 v[100:101], v[130:131], v[100:101]
	s_waitcnt vmcnt(4)
	v_pk_mul_f32 v[104:105], v[134:135], v[104:105]
	v_pk_mul_f32 v[106:107], v[136:137], v[106:107]
	s_waitcnt vmcnt(2)
	v_pk_add_f32 v[134:135], v[144:145], 1.0 op_sel_hi:[1,0]
	v_pk_add_f32 v[136:137], v[142:143], 1.0 op_sel_hi:[1,0]
	v_pk_mul_f32 v[102:103], v[132:133], v[102:103]
	v_pk_add_f32 v[130:131], v[140:141], 1.0 op_sel_hi:[1,0]
	v_pk_add_f32 v[132:133], v[138:139], 1.0 op_sel_hi:[1,0]
	s_waitcnt vmcnt(0)
	v_pk_fma_f32 v[106:107], v[134:135], v[106:107], v[152:153]
	v_pk_fma_f32 v[104:105], v[136:137], v[104:105], v[150:151]
	v_pk_fma_f32 v[130:131], v[130:131], v[102:103], v[148:149]
	v_pk_fma_f32 v[102:103], v[132:133], v[100:101], v[146:147]
	v_cvt_pk_bf16_f32 v100, v104, v105
	v_cvt_pk_bf16_f32 v101, v106, v107
	v_cvt_pk_bf16_f32 v102, v102, v103
	v_cvt_pk_bf16_f32 v103, v130, v131
	v_lshl_add_u64 v[146:147], v[128:129], 0, s[18:19]
	global_store_dwordx4 v[146:147], v[100:103], off
	global_load_dwordx4 v[100:103], v[124:125], off offset:2064
	s_nop 0
	global_load_dwordx4 v[104:107], v[124:125], off offset:2048
	global_load_dwordx4 v[130:133], v123, s[16:17] offset:16
	global_load_dwordx4 v[134:137], v123, s[16:17]
	global_load_dwordx4 v[138:141], v117, s[14:15] offset:2064
	global_load_dwordx4 v[142:145], v117, s[14:15] offset:2048
	s_waitcnt vmcnt(5)
	v_pk_mul_f32 v[100:101], v[100:101], v[108:109]
	s_waitcnt vmcnt(4)
	v_pk_mul_f32 v[104:105], v[104:105], v[112:113]
	v_pk_mul_f32 v[106:107], v[106:107], v[114:115]
	s_waitcnt vmcnt(2)
	v_pk_add_f32 v[112:113], v[136:137], 1.0 op_sel_hi:[1,0]
	v_pk_add_f32 v[114:115], v[134:135], 1.0 op_sel_hi:[1,0]
	v_pk_mul_f32 v[102:103], v[102:103], v[110:111]
	v_pk_add_f32 v[108:109], v[132:133], 1.0 op_sel_hi:[1,0]
	v_pk_add_f32 v[110:111], v[130:131], 1.0 op_sel_hi:[1,0]
	s_waitcnt vmcnt(0)
	v_pk_fma_f32 v[106:107], v[112:113], v[106:107], v[144:145]
	v_pk_fma_f32 v[104:105], v[114:115], v[104:105], v[142:143]
	v_pk_fma_f32 v[108:109], v[108:109], v[102:103], v[140:141]
	v_pk_fma_f32 v[102:103], v[110:111], v[100:101], v[138:139]
	v_cvt_pk_bf16_f32 v100, v104, v105
	v_cvt_pk_bf16_f32 v101, v106, v107
	v_cvt_pk_bf16_f32 v102, v102, v103
	v_cvt_pk_bf16_f32 v103, v108, v109
	global_store_dwordx4 v[146:147], v[100:103], off offset:1024
.LBB0_3038:
	s_andn2_b64 vcc, exec, s[12:13]
	s_mov_b64 s[12:13], 0
	s_cbranch_vccnz .LBB0_3035
	s_add_i32 s4, s6, 0x1000
	s_cmp_lt_i32 s4, s36
	s_cselect_b64 s[12:13], -1, 0
	s_and_b64 s[14:15], s[12:13], exec
	s_cselect_b32 s14, s4, s10
	s_ashr_i32 s15, s14, 31
	s_min_i32 s7, s10, 0x4000
	s_lshl_b64 s[16:17], s[14:15], 13
	s_lshl_b64 s[14:15], s[14:15], 12
	s_ashr_i32 s7, s7, 12
	s_waitcnt vmcnt(4)
	v_lshlrev_b32_e32 v100, 16, v94
	v_and_b32_e32 v101, 0xffff0000, v94
	v_lshlrev_b32_e32 v94, 16, v95
	v_and_b32_e32 v95, 0xffff0000, v95
	v_lshl_add_u64 v[46:47], v[120:121], 0, s[14:15]
	s_mul_hi_i32 s15, s7, 0x1800
	s_mul_i32 s14, s7, 0x1800
	v_pk_add_f32 v[94:95], v[94:95], 0 op_sel_hi:[1,0]
	v_lshlrev_b32_e32 v102, 16, v96
	v_and_b32_e32 v103, 0xffff0000, v96
	v_lshlrev_b32_e32 v96, 16, v97
	v_and_b32_e32 v97, 0xffff0000, v97
	v_lshlrev_b32_e32 v104, 16, v90
	v_and_b32_e32 v105, 0xffff0000, v90
	v_lshlrev_b32_e32 v90, 16, v91
	v_and_b32_e32 v91, 0xffff0000, v91
	s_lshl_b64 s[14:15], s[14:15], 2
	v_pk_add_f32 v[100:101], v[100:101], 0 op_sel_hi:[1,0]
	v_pk_add_f32 v[96:97], v[96:97], 0 op_sel_hi:[1,0]
	v_pk_add_f32 v[90:91], v[94:95], v[90:91]
	v_lshlrev_b32_e32 v94, 16, v92
	v_and_b32_e32 v95, 0xffff0000, v92
	v_lshlrev_b32_e32 v92, 16, v93
	v_and_b32_e32 v93, 0xffff0000, v93
	s_add_u32 s7, s37, s14
	v_pk_add_f32 v[102:103], v[102:103], 0 op_sel_hi:[1,0]
	v_pk_add_f32 v[100:101], v[100:101], v[104:105]
	v_pk_add_f32 v[92:93], v[96:97], v[92:93]
	v_lshlrev_b32_e32 v96, 16, v86
	v_and_b32_e32 v97, 0xffff0000, v86
	v_lshlrev_b32_e32 v86, 16, v87
	v_and_b32_e32 v87, 0xffff0000, v87
	v_lshl_add_u64 v[30:31], v[118:119], 0, s[16:17]
	s_addc_u32 s11, s38, s15
	v_pk_add_f32 v[94:95], v[102:103], v[94:95]
	v_pk_add_f32 v[86:87], v[90:91], v[86:87]
	v_pk_add_f32 v[90:91], v[100:101], v[96:97]
	v_lshlrev_b32_e32 v96, 16, v88
	v_and_b32_e32 v97, 0xffff0000, v88
	v_lshlrev_b32_e32 v88, 16, v89
	v_and_b32_e32 v89, 0xffff0000, v89
	v_add_co_u32_e32 v38, vcc, 0x1000, v30
	s_add_u32 s16, s7, 0x5000
	v_pk_add_f32 v[88:89], v[92:93], v[88:89]
	v_pk_add_f32 v[92:93], v[94:95], v[96:97]
	v_lshlrev_b32_e32 v94, 16, v82
	v_and_b32_e32 v95, 0xffff0000, v82
	v_lshlrev_b32_e32 v96, 16, v83
	v_and_b32_e32 v97, 0xffff0000, v83
	v_addc_co_u32_e32 v39, vcc, 0, v31, vcc
	s_addc_u32 s17, s11, 0
	v_pk_add_f32 v[82:83], v[90:91], v[94:95]
	v_pk_add_f32 v[94:95], v[86:87], v[96:97]
	v_lshlrev_b32_e32 v86, 16, v84
	v_and_b32_e32 v87, 0xffff0000, v84
	v_lshlrev_b32_e32 v84, 16, v85
	v_and_b32_e32 v85, 0xffff0000, v85
	v_pk_add_f32 v[92:93], v[92:93], v[86:87]
	v_pk_add_f32 v[96:97], v[88:89], v[84:85]
	global_load_dwordx4 v[84:87], v117, s[16:17] offset:16
	global_load_dwordx4 v[88:91], v117, s[16:17]
	global_load_dwordx4 v[162:165], v123, s[16:17] offset:16
	global_load_dwordx4 v[166:169], v123, s[16:17]
	global_load_dwordx4 v[2:5], v[30:31], off nt
	global_load_dwordx4 v[14:17], v[30:31], off offset:2048 nt
	global_load_dwordx4 v[18:21], v[38:39], off nt
	global_load_dwordx4 v[26:29], v[38:39], off offset:2048 nt
	global_load_dwordx4 v[6:9], v[46:47], off offset:16
	global_load_dwordx4 v[10:13], v[46:47], off
	global_load_dwordx4 v[22:25], v[30:31], off offset:1024 nt
	s_nop 0
	global_load_dwordx4 v[30:33], v[30:31], off offset:3072 nt
	s_nop 0
	global_load_dwordx4 v[34:37], v[38:39], off offset:1024 nt
	s_nop 0
	global_load_dwordx4 v[38:41], v[38:39], off offset:3072 nt
	s_nop 0
	global_load_dwordx4 v[42:45], v[46:47], off offset:2064
	s_nop 0
	global_load_dwordx4 v[46:49], v[46:47], off offset:2048
	s_ashr_i32 s11, s10, 31
	s_lshl_b64 s[18:19], s[10:11], 12
	s_and_b64 vcc, exec, s[34:35]
	s_waitcnt vmcnt(15)
	v_pk_fma_f32 v[74:75], v[92:93], v[84:85], v[74:75]
	v_lshlrev_b32_e32 v84, 16, v70
	v_and_b32_e32 v85, 0xffff0000, v70
	v_lshlrev_b32_e32 v70, 16, v71
	v_and_b32_e32 v71, 0xffff0000, v71
	s_waitcnt vmcnt(14)
	v_pk_fma_f32 v[78:79], v[82:83], v[88:89], v[78:79]
	v_pk_fma_f32 v[76:77], v[96:97], v[86:87], v[76:77]
	v_pk_add_f32 v[70:71], v[70:71], 0 op_sel_hi:[1,0]
	v_lshlrev_b32_e32 v86, 16, v72
	v_and_b32_e32 v87, 0xffff0000, v72
	v_lshlrev_b32_e32 v72, 16, v73
	v_and_b32_e32 v73, 0xffff0000, v73
	v_lshlrev_b32_e32 v88, 16, v66
	v_and_b32_e32 v89, 0xffff0000, v66
	v_lshlrev_b32_e32 v66, 16, v67
	v_and_b32_e32 v67, 0xffff0000, v67
	v_pk_add_f32 v[84:85], v[84:85], 0 op_sel_hi:[1,0]
	v_pk_add_f32 v[72:73], v[72:73], 0 op_sel_hi:[1,0]
	v_pk_add_f32 v[66:67], v[70:71], v[66:67]
	v_lshlrev_b32_e32 v70, 16, v68
	v_and_b32_e32 v71, 0xffff0000, v68
	v_lshlrev_b32_e32 v68, 16, v69
	v_and_b32_e32 v69, 0xffff0000, v69
	v_pk_add_f32 v[86:87], v[86:87], 0 op_sel_hi:[1,0]
	v_pk_add_f32 v[84:85], v[84:85], v[88:89]
	v_pk_add_f32 v[68:69], v[72:73], v[68:69]
	v_lshlrev_b32_e32 v72, 16, v62
	v_and_b32_e32 v73, 0xffff0000, v62
	v_lshlrev_b32_e32 v62, 16, v63
	v_and_b32_e32 v63, 0xffff0000, v63
	v_pk_add_f32 v[70:71], v[86:87], v[70:71]
	v_pk_add_f32 v[62:63], v[66:67], v[62:63]
	v_pk_add_f32 v[66:67], v[84:85], v[72:73]
	v_lshlrev_b32_e32 v72, 16, v64
	v_and_b32_e32 v73, 0xffff0000, v64
	v_lshlrev_b32_e32 v64, 16, v65
	v_and_b32_e32 v65, 0xffff0000, v65
	v_pk_fma_f32 v[80:81], v[94:95], v[90:91], v[80:81]
	v_lshl_add_u64 v[82:83], v[126:127], 0, s[18:19]
	v_pk_add_f32 v[64:65], v[68:69], v[64:65]
	v_pk_add_f32 v[68:69], v[70:71], v[72:73]
	v_lshlrev_b32_e32 v70, 16, v58
	v_and_b32_e32 v71, 0xffff0000, v58
	v_lshlrev_b32_e32 v58, 16, v59
	v_and_b32_e32 v59, 0xffff0000, v59
	global_store_dwordx4 v[82:83], v[78:81], off
	global_store_dwordx4 v[82:83], v[74:77], off offset:16
	v_pk_add_f32 v[66:67], v[66:67], v[70:71]
	v_pk_add_f32 v[70:71], v[62:63], v[58:59]
	v_lshlrev_b32_e32 v58, 16, v60
	v_and_b32_e32 v59, 0xffff0000, v60
	v_lshlrev_b32_e32 v60, 16, v61
	v_and_b32_e32 v61, 0xffff0000, v61
	v_pk_add_f32 v[68:69], v[68:69], v[58:59]
	v_pk_add_f32 v[72:73], v[64:65], v[60:61]
	s_waitcnt vmcnt(14)
	v_pk_fma_f32 v[52:53], v[72:73], v[164:165], v[52:53]
	v_pk_fma_f32 v[56:57], v[70:71], v[168:169], v[56:57]
	v_pk_fma_f32 v[54:55], v[66:67], v[166:167], v[54:55]
	v_pk_fma_f32 v[50:51], v[68:69], v[162:163], v[50:51]
	global_store_dwordx4 v[82:83], v[54:57], off offset:2048
	global_store_dwordx4 v[82:83], v[50:53], off offset:2064
	s_cbranch_vccnz .LBB0_3034
	v_pk_mul_f32 v[58:59], v[80:81], v[80:81]
	v_pk_mul_f32 v[60:61], v[78:79], v[78:79]
	s_add_u32 s14, s39, s14
	v_pk_mov_b32 v[62:63], v[60:61], v[58:59] op_sel:[1,0]
	v_mov_b32_e32 v61, v59
	v_pk_add_f32 v[58:59], v[62:63], v[60:61]
	v_pk_mul_f32 v[60:61], v[76:77], v[76:77]
	v_pk_mul_f32 v[62:63], v[74:75], v[74:75]
	v_pk_add_f32 v[58:59], v[58:59], v[58:59] op_sel:[0,1] op_sel_hi:[1,0]
	v_pk_mov_b32 v[64:65], v[62:63], v[60:61] op_sel:[1,0]
	v_mov_b32_e32 v63, v61
	v_pk_add_f32 v[60:61], v[64:65], v[62:63]
	v_mul_f32_e32 v62, v50, v50
	v_mul_f32_e32 v63, v51, v51
	v_pk_add_f32 v[60:61], v[60:61], v[60:61] op_sel:[0,1] op_sel_hi:[1,0]
	v_mov_b32_e32 v59, v62
	v_mov_b32_e32 v61, v63
	v_pk_add_f32 v[58:59], v[58:59], v[60:61]
	v_mul_f32_e32 v60, v55, v55
	v_mul_f32_e32 v62, v57, v57
	v_mul_f32_e32 v64, v52, v52
	v_mul_f32_e32 v65, v53, v53
	v_pk_fma_f32 v[60:61], v[54:55], v[54:55], v[60:61] op_sel_hi:[1,1,0]
	v_pk_fma_f32 v[62:63], v[56:57], v[56:57], v[62:63] op_sel_hi:[1,1,0]
	v_mov_b32_e32 v61, v64
	v_mov_b32_e32 v63, v65
	v_pk_add_f32 v[60:61], v[60:61], v[62:63]
	s_addc_u32 s15, s40, s15
	v_pk_add_f32 v[58:59], v[58:59], v[60:61]
	v_and_b32_e32 v60, 64, v214
	v_add_f32_e32 v58, v58, v59
	v_xor_b32_e32 v59, 16, v214
	v_add_u32_e32 v60, 64, v60
	v_add_f32_dpp v58, v58, v58 quad_perm:[1,0,3,2] row_mask:0xf bank_mask:0xf bound_ctrl:1
	v_cmp_lt_i32_e32 vcc, v59, v60
	s_add_u32 s16, s14, 0x1000
	v_add_f32_dpp v58, v58, v58 quad_perm:[2,3,0,1] row_mask:0xf bank_mask:0xf bound_ctrl:1
	v_cndmask_b32_e32 v59, v214, v59, vcc
	v_lshlrev_b32_e32 v59, 2, v59
	v_add_f32_dpp v58, v58, v58 row_half_mirror row_mask:0xf bank_mask:0xf bound_ctrl:1
	s_addc_u32 s17, s15, 0
	s_lshl_b64 s[10:11], s[10:11], 11
	v_add_f32_dpp v58, v58, v58 row_mirror row_mask:0xf bank_mask:0xf bound_ctrl:1
	ds_bpermute_b32 v59, v59, v58
	s_waitcnt lgkmcnt(0)
	v_add_f32_e32 v58, v58, v59
	v_xor_b32_e32 v59, 32, v214
	v_cmp_lt_i32_e32 vcc, v59, v60
	s_nop 1
	v_cndmask_b32_e32 v59, v214, v59, vcc
	v_lshlrev_b32_e32 v59, 2, v59
	ds_bpermute_b32 v59, v59, v58
	s_waitcnt lgkmcnt(0)
	v_add_f32_e32 v58, v58, v59
	v_fmamk_f32 v58, v58, 0x3a800000, v1
	v_cmp_gt_f32_e32 vcc, s77, v58
	v_mul_f32_e32 v59, 0x4b800000, v58
	s_nop 0
	v_cndmask_b32_e32 v58, v58, v59, vcc
	v_rsq_f32_e32 v58, v58
	s_nop 0
	v_mul_f32_e32 v59, 0x45800000, v58
	v_cndmask_b32_e32 v62, v58, v59, vcc
	global_load_dwordx4 v[58:61], v[124:125], off offset:16
	global_load_dwordx4 v[64:67], v[124:125], off
	global_load_dwordx4 v[68:71], v117, s[16:17] offset:16
	global_load_dwordx4 v[82:85], v117, s[16:17]
	global_load_dwordx4 v[86:89], v117, s[14:15] offset:16
	global_load_dwordx4 v[90:93], v117, s[14:15]
	v_pk_mul_f32 v[72:73], v[80:81], v[62:63] op_sel_hi:[1,0]
	v_pk_mul_f32 v[78:79], v[78:79], v[62:63] op_sel_hi:[1,0]
	v_pk_mul_f32 v[74:75], v[74:75], v[62:63] op_sel_hi:[1,0]
	v_pk_mul_f32 v[56:57], v[56:57], v[62:63] op_sel_hi:[1,0]
	v_pk_mul_f32 v[54:55], v[54:55], v[62:63] op_sel_hi:[1,0]
	v_pk_mul_f32 v[52:53], v[52:53], v[62:63] op_sel_hi:[1,0]
	v_pk_mul_f32 v[50:51], v[50:51], v[62:63] op_sel_hi:[1,0]
	s_waitcnt vmcnt(5)
	v_pk_mul_f32 v[58:59], v[58:59], v[74:75]
	s_waitcnt vmcnt(4)
	v_pk_mul_f32 v[66:67], v[66:67], v[72:73]
	v_pk_mul_f32 v[64:65], v[64:65], v[78:79]
	s_waitcnt vmcnt(2)
	v_pk_add_f32 v[72:73], v[84:85], 1.0 op_sel_hi:[1,0]
	v_pk_add_f32 v[78:79], v[82:83], 1.0 op_sel_hi:[1,0]
	s_waitcnt vmcnt(0)
	v_pk_fma_f32 v[66:67], v[72:73], v[66:67], v[92:93]
	v_pk_mul_f32 v[72:73], v[76:77], v[62:63] op_sel_hi:[1,0]
	v_pk_add_f32 v[70:71], v[70:71], 1.0 op_sel_hi:[1,0]
	v_pk_mul_f32 v[60:61], v[60:61], v[72:73]
	v_pk_add_f32 v[68:69], v[68:69], 1.0 op_sel_hi:[1,0]
	v_pk_fma_f32 v[64:65], v[78:79], v[64:65], v[90:91]
	v_pk_fma_f32 v[70:71], v[70:71], v[60:61], v[88:89]
	v_pk_fma_f32 v[60:61], v[68:69], v[58:59], v[86:87]
	v_cvt_pk_bf16_f32 v58, v64, v65
	v_cvt_pk_bf16_f32 v59, v66, v67
	v_cvt_pk_bf16_f32 v60, v60, v61
	v_cvt_pk_bf16_f32 v61, v70, v71
	v_lshl_add_u64 v[84:85], v[128:129], 0, s[10:11]
	global_store_dwordx4 v[84:85], v[58:61], off
	global_load_dwordx4 v[58:61], v[124:125], off offset:2064
	s_nop 0
	global_load_dwordx4 v[64:67], v[124:125], off offset:2048
	global_load_dwordx4 v[68:71], v123, s[16:17] offset:16
	global_load_dwordx4 v[72:75], v123, s[16:17]
	global_load_dwordx4 v[76:79], v117, s[14:15] offset:2064
	global_load_dwordx4 v[80:83], v117, s[14:15] offset:2048
	s_waitcnt vmcnt(5)
	v_pk_mul_f32 v[50:51], v[58:59], v[50:51]
	s_waitcnt vmcnt(4)
	v_pk_mul_f32 v[54:55], v[64:65], v[54:55]
	v_pk_mul_f32 v[56:57], v[66:67], v[56:57]
	s_waitcnt vmcnt(2)
	v_pk_add_f32 v[64:65], v[74:75], 1.0 op_sel_hi:[1,0]
	v_pk_add_f32 v[66:67], v[72:73], 1.0 op_sel_hi:[1,0]
	v_pk_mul_f32 v[52:53], v[60:61], v[52:53]
	v_pk_add_f32 v[58:59], v[70:71], 1.0 op_sel_hi:[1,0]
	v_pk_add_f32 v[60:61], v[68:69], 1.0 op_sel_hi:[1,0]
	s_waitcnt vmcnt(0)
	v_pk_fma_f32 v[56:57], v[64:65], v[56:57], v[82:83]
	v_pk_fma_f32 v[54:55], v[66:67], v[54:55], v[80:81]
	v_pk_fma_f32 v[58:59], v[58:59], v[52:53], v[78:79]
	v_pk_fma_f32 v[52:53], v[60:61], v[50:51], v[76:77]
	v_cvt_pk_bf16_f32 v50, v54, v55
	v_cvt_pk_bf16_f32 v51, v56, v57
	v_cvt_pk_bf16_f32 v52, v52, v53
	v_cvt_pk_bf16_f32 v53, v58, v59
	global_store_dwordx4 v[84:85], v[50:53], off offset:1024
	s_branch .LBB0_3034
.LBB0_3041:
	s_waitcnt vmcnt(0)
	v_readlane_b32 s6, v251, 0
	s_add_i32 s4, s48, 4
	v_readlane_b32 s7, v251, 1
	s_cmp_lt_i32 s4, s7
	s_cselect_b64 s[6:7], -1, 0
	s_and_b64 s[2:3], s[2:3], s[6:7]
	v_writelane_b32 v254, s4, 36
	s_andn2_b64 vcc, exec, s[2:3]
	s_cbranch_vccz .LBB0_3042
	s_getpc_b64 s[98:99]
